# v65 + LayerNorm wave reductions: the two cross-row hops (xor 32, xor 16) via v_permlane32_swap / v_permlane16_swap on a copy instead of ds_bpermute round trips (no LDS round trip left in the P4/P7 row
# speedup vs baseline: 1.0119x; 1.0085x over previous
; DI float bflo(unsigned w) { return __uint_as_float(w << 16); }
; DI float bfhi(unsigned w) { return __uint_as_float(w & 0xffff0000u); }
; DI void p4_ln_router(const Ctx& c) {
;     ...
;         for (int tt = 0; tt < 2; ++tt) { const int tl = 2 * w + tt, tok = tokbase + pass * 16 + tl;
;             const u32x2* src = (const u32x2*)(y1 + (size_t)tok * D); f32x4 v[8]; float s = 0.f;
; #pragma unroll
;             for (int i = 0; i < 8; ++i) { const u32x2 yv = src[i * 64 + lane]; v[i] = (f32x4){bflo(yv.x), bfhi(yv.x), bflo(yv.y), bfhi(yv.y)}; s += (v[i][0] + v[i][1]) + (v[i][2] + v[i][3]); }
.LBB0_443:
	s_or_b32 s36, s24, s5
	s_add_i32 s24, s31, s36
	s_ashr_i32 s25, s24, 31
	s_lshl_b64 s[26:27], s[24:25], 12
	v_lshl_add_u64 v[0:1], v[50:51], 0, s[26:27]
	global_load_dwordx2 v[2:3], v[0:1], off offset:512
	global_load_dwordx2 v[4:5], v[0:1], off
	global_load_dwordx2 v[6:7], v[0:1], off offset:1024
	global_load_dwordx2 v[8:9], v[0:1], off offset:1536
	global_load_dwordx2 v[10:11], v[0:1], off offset:2048
	global_load_dwordx2 v[12:13], v[0:1], off offset:2560
	global_load_dwordx2 v[68:69], v[0:1], off offset:3072
	global_load_dwordx2 v[70:71], v[0:1], off offset:3584
	s_waitcnt vmcnt(7)
	v_lshlrev_b32_e32 v63, 16, v2
	s_waitcnt vmcnt(6)
	v_lshlrev_b32_e32 v62, 16, v4
	v_and_b32_e32 v61, 0xffff0000, v2
	v_and_b32_e32 v60, 0xffff0000, v4
	v_lshlrev_b32_e32 v67, 16, v3
	v_lshlrev_b32_e32 v66, 16, v5
	v_and_b32_e32 v65, 0xffff0000, v3
	v_and_b32_e32 v64, 0xffff0000, v5
	s_waitcnt vmcnt(5)
	v_lshlrev_b32_e32 v57, 16, v7
	v_lshlrev_b32_e32 v56, 16, v6
	v_and_b32_e32 v59, 0xffff0000, v7
	v_and_b32_e32 v58, 0xffff0000, v6
	s_waitcnt vmcnt(4)
	v_lshlrev_b32_e32 v22, 16, v8
	v_and_b32_e32 v23, 0xffff0000, v8
	v_lshlrev_b32_e32 v54, 16, v9
	v_and_b32_e32 v55, 0xffff0000, v9
	s_waitcnt vmcnt(1)
	v_lshlrev_b32_e32 v6, 16, v68
	v_and_b32_e32 v7, 0xffff0000, v68
	v_lshlrev_b32_e32 v8, 16, v69
	v_and_b32_e32 v9, 0xffff0000, v69
	s_waitcnt vmcnt(0)
; DI float bflo(unsigned w) { return __uint_as_float(w << 16); }
; DI float bfhi(unsigned w) { return __uint_as_float(w & 0xffff0000u); }
; DI void p4_ln_router(const Ctx& c) {
;     ...
;             for (int i = 0; i < 8; ++i) { const u32x2 yv = src[i * 64 + lane]; v[i] = (f32x4){bflo(yv.x), bfhi(yv.x), bflo(yv.y), bfhi(yv.y)}; s += (v[i][0] + v[i][1]) + (v[i][2] + v[i][3]); }
; #pragma unroll
;             for (int o = 32; o >= 1; o >>= 1) s += __shfl_xor(s, o);
;             const float mean = s * (1.0f / D); float qv = 0.f;
; #pragma unroll
;             for (int i = 0; i < 8; ++i) { const f32x4 dl = v[i] - mean; qv += (dl[0] * dl[0] + dl[1] * dl[1]) + (dl[2] * dl[2] + dl[3] * dl[3]); }
; #pragma unroll
;             for (int o = 32; o >= 1; o >>= 1) qv += __shfl_xor(qv, o);
;             const float rstd = rsqrtf(qv * (1.0f / D) + LN_EPS);
;             if (lane == 0) { st1[2 * tok] = mean; st1[2 * tok + 1] = rstd; }
	v_lshlrev_b32_e32 v2, 16, v70
	v_and_b32_e32 v3, 0xffff0000, v70
	v_lshlrev_b32_e32 v5, 16, v71
	v_and_b32_e32 v1, 0xffff0000, v71
	v_pk_add_f32 v[68:69], v[62:63], v[60:61]
	v_pk_add_f32 v[70:71], v[66:67], v[64:65]
	v_pk_add_f32 v[72:73], v[56:57], v[58:59]
	v_add_f32_e32 v4, v6, v7
	v_add_f32_e32 v0, v8, v9
	v_pk_add_f32 v[68:69], v[68:69], v[70:71]
	v_and_b32_e32 v15, 0xffff0000, v10
	v_pk_add_f32 v[70:71], v[72:73], v[72:73] op_sel:[0,1] op_sel_hi:[1,0]
	v_pk_add_f32 v[76:77], v[4:5], v[0:1]
	v_add_f32_e32 v0, 0, v68
	v_lshlrev_b32_e32 v19, 16, v10
	v_lshlrev_b32_e32 v21, 16, v11
	v_and_b32_e32 v17, 0xffff0000, v11
	v_add_f32_e32 v20, v22, v23
	v_add_f32_e32 v16, v54, v55
	v_mov_b32_e32 v71, v15
	v_add_f32_e32 v18, v0, v69
	v_lshlrev_b32_e32 v11, 16, v13
	v_lshlrev_b32_e32 v10, 16, v12
	v_and_b32_e32 v13, 0xffff0000, v13
	v_and_b32_e32 v12, 0xffff0000, v12
	v_pk_add_f32 v[72:73], v[20:21], v[16:17]
	v_pk_add_f32 v[68:69], v[18:19], v[70:71]
	v_pk_add_f32 v[74:75], v[10:11], v[12:13]
	v_pk_add_f32 v[68:69], v[68:69], v[72:73]
	v_pk_add_f32 v[74:75], v[74:75], v[74:75] op_sel:[0,1] op_sel_hi:[1,0]
	v_pk_add_f32 v[68:69], v[68:69], v[68:69] op_sel:[0,1] op_sel_hi:[1,0]
	v_mov_b32_e32 v75, v3
	v_mov_b32_e32 v69, v2
	v_pk_add_f32 v[68:69], v[68:69], v[74:75]
	s_nop 0
	v_pk_add_f32 v[68:69], v[68:69], v[76:77]
	s_nop 0
	v_add_f32_e32 v0, v68, v69
	v_mov_b32_e32 v4, v0
	s_nop 1
	v_permlane32_swap_b32 v0, v4
	v_add_f32_e32 v0, v0, v4
	v_mov_b32_e32 v4, v0
	s_nop 1
	v_permlane16_swap_b32 v0, v4
	v_add_f32_e32 v0, v0, v4
	s_nop 1
	v_add_f32_dpp v0, v0, v0 row_ror:8 row_mask:0xf bank_mask:0xf
	s_nop 1
	v_add_f32_dpp v0, v0, v0 row_ror:4 row_mask:0xf bank_mask:0xf
	s_nop 1
	v_add_f32_dpp v0, v0, v0 quad_perm:[2,3,0,1] row_mask:0xf bank_mask:0xf
	s_nop 1
	v_add_f32_dpp v0, v0, v0 quad_perm:[1,0,3,2] row_mask:0xf bank_mask:0xf
	v_fmac_f32_e32 v64, 0xba000000, v0
	v_fmac_f32_e32 v60, 0xba000000, v0
	v_fmac_f32_e32 v65, 0xba000000, v0
	v_fmac_f32_e32 v61, 0xba000000, v0
	v_fmac_f32_e32 v59, 0xba000000, v0
	v_fmac_f32_e32 v57, 0xba000000, v0
	v_fmac_f32_e32 v58, 0xba000000, v0
	v_fmac_f32_e32 v66, 0xba000000, v0
	v_fmac_f32_e32 v62, 0xba000000, v0
	v_fmac_f32_e32 v67, 0xba000000, v0
	v_fmac_f32_e32 v63, 0xba000000, v0
	v_fmac_f32_e32 v56, 0xba000000, v0
	v_pk_mul_f32 v[68:69], v[60:61], v[60:61]
	v_pk_mul_f32 v[72:73], v[64:65], v[64:65]
	v_mov_b32_e32 v78, v57
	v_mov_b32_e32 v79, v59
	v_mov_b32_e32 v57, v58
	v_pk_fma_f32 v[68:69], v[62:63], v[62:63], v[68:69]
	v_pk_fma_f32 v[72:73], v[66:67], v[66:67], v[72:73]
	v_pk_mul_f32 v[74:75], v[78:79], v[78:79]
	v_pk_mul_f32 v[76:77], v[56:57], v[56:57]
	v_fmac_f32_e32 v54, 0xba000000, v0
	v_fmac_f32_e32 v22, 0xba000000, v0
	v_pk_add_f32 v[68:69], v[68:69], v[72:73]
	v_pk_mov_b32 v[72:73], v[76:77], v[74:75] op_sel:[1,0]
	v_mov_b32_e32 v77, v75
	v_fmac_f32_e32 v55, 0xba000000, v0
	v_fmac_f32_e32 v23, 0xba000000, v0
	v_fmac_f32_e32 v15, 0xba000000, v0
	v_fmac_f32_e32 v13, 0xba000000, v0
	v_fmac_f32_e32 v11, 0xba000000, v0
	v_fmac_f32_e32 v12, 0xba000000, v0
	v_mul_f32_e32 v4, v22, v22
	v_mul_f32_e32 v14, v54, v54
	v_pk_add_f32 v[72:73], v[72:73], v[76:77]
	v_fmac_f32_e32 v17, 0xba000000, v0
	v_fmac_f32_e32 v21, 0xba000000, v0
	v_fmac_f32_e32 v19, 0xba000000, v0
	v_fmac_f32_e32 v10, 0xba000000, v0
	v_mov_b32_e32 v70, v11
	v_mov_b32_e32 v71, v13
	v_mov_b32_e32 v11, v12
	v_pk_fma_f32 v[116:117], v[22:23], v[22:23], v[4:5] op_sel_hi:[1,1,0]
	v_pk_fma_f32 v[118:119], v[54:55], v[54:55], v[14:15] op_sel_hi:[1,1,0]
	v_pk_add_f32 v[68:69], v[68:69], v[68:69] op_sel_hi:[0,1]
	v_pk_add_f32 v[72:73], v[72:73], v[72:73] op_sel_hi:[0,1]
	v_pk_mul_f32 v[120:121], v[70:71], v[70:71]
	v_pk_mul_f32 v[122:123], v[10:11], v[10:11]
	v_mul_f32_e32 v116, v19, v19
	v_mul_f32_e32 v118, v15, v15
	v_mul_f32_e32 v68, v17, v17
	v_mul_f32_e32 v72, v21, v21
	v_fmac_f32_e32 v6, 0xba000000, v0
	v_fmac_f32_e32 v8, 0xba000000, v0
	v_pk_mov_b32 v[74:75], v[122:123], v[120:121] op_sel:[1,0]
	v_mov_b32_e32 v123, v121
	v_pk_add_f32 v[76:77], v[116:117], v[118:119]
	v_pk_add_f32 v[68:69], v[72:73], v[68:69]
	v_fmac_f32_e32 v7, 0xba000000, v0
	v_mul_f32_e32 v4, v6, v6
	v_fmac_f32_e32 v9, 0xba000000, v0
	v_pk_add_f32 v[74:75], v[74:75], v[122:123]
	v_pk_add_f32 v[68:69], v[76:77], v[68:69]
	v_pk_fma_f32 v[72:73], v[6:7], v[6:7], v[4:5] op_sel_hi:[1,1,0]
	v_mul_f32_e32 v4, v8, v8
	v_pk_add_f32 v[74:75], v[74:75], v[74:75] op_sel_hi:[0,1]
	v_pk_add_f32 v[68:69], v[68:69], v[68:69] op_sel_hi:[0,1]
	v_pk_fma_f32 v[76:77], v[8:9], v[8:9], v[4:5] op_sel_hi:[1,1,0]
	v_fmac_f32_e32 v1, 0xba000000, v0
	v_fmac_f32_e32 v5, 0xba000000, v0
	v_fmac_f32_e32 v3, 0xba000000, v0
	v_fmac_f32_e32 v2, 0xba000000, v0
	v_mul_f32_e32 v72, v2, v2
	v_mul_f32_e32 v76, v3, v3
	v_mul_f32_e32 v74, v5, v5
	v_mul_f32_e32 v68, v1, v1
	v_pk_add_f32 v[72:73], v[72:73], v[76:77]
	v_pk_add_f32 v[68:69], v[74:75], v[68:69]
	s_nop 0
	v_pk_add_f32 v[68:69], v[72:73], v[68:69]
	s_nop 0
	v_add_f32_e32 v4, v68, v69
	v_mov_b32_e32 v11, v4
	s_nop 1
	v_permlane32_swap_b32 v4, v11
	v_add_f32_e32 v4, v4, v11
	v_mov_b32_e32 v11, v4
	s_nop 1
	v_permlane16_swap_b32 v4, v11
	v_add_f32_e32 v4, v4, v11
	s_nop 1
	v_add_f32_dpp v4, v4, v4 row_ror:8 row_mask:0xf bank_mask:0xf
	s_nop 1
	v_add_f32_dpp v4, v4, v4 row_ror:4 row_mask:0xf bank_mask:0xf
	s_nop 1
	v_add_f32_dpp v4, v4, v4 quad_perm:[2,3,0,1] row_mask:0xf bank_mask:0xf
	s_nop 1
	v_add_f32_dpp v4, v4, v4 quad_perm:[1,0,3,2] row_mask:0xf bank_mask:0xf
	v_fmamk_f32 v4, v4, 0x3a000000, v110
	v_mul_f32_e32 v11, 0x4b800000, v4
	v_cmp_gt_f32_e32 vcc, s6, v4
	s_nop 1
	v_cndmask_b32_e32 v4, v4, v11, vcc
	v_rsq_f32_e32 v4, v4
	s_nop 0
	v_mul_f32_e32 v11, 0x45800000, v4
	v_cndmask_b32_e32 v4, v4, v11, vcc
	s_and_saveexec_b64 s[26:27], s[10:11]
	s_cbranch_execz .LBB0_442
	s_lshl_b32 s38, s24, 1
	s_ashr_i32 s39, s38, 31
	s_lshl_b64 s[38:39], s[38:39], 2
	s_add_u32 s38, s3, s38
	v_mul_f32_e32 v68, 0x3a000000, v0
	s_addc_u32 s39, s71, s39
	v_mov_b32_e32 v69, v4
	global_store_dwordx2 v25, v[68:69], s[38:39]
	s_branch .LBB0_442

; DI float bflo(unsigned w) { return __uint_as_float(w << 16); }
; DI float bfhi(unsigned w) { return __uint_as_float(w & 0xffff0000u); }
; DI void p7_ln2(const Ctx& c) {
;     ...
;         for (int i = 0; i < 4; ++i) { const int d = (i * 64 + lane) * 8; const u32x4 yr = *(const u32x4*)(y1 + (size_t)tok * D + d);
;             const f32x4 y0 = {bflo(yr.x), bfhi(yr.x), bflo(yr.y), bfhi(yr.y)}, y1v = {bflo(yr.z), bfhi(yr.z), bflo(yr.w), bfhi(yr.w)};
;             const f32x4 g0 = *(const f32x4*)(l1w + d), g1 = *(const f32x4*)(l1w + d + 4), b0 = *(const f32x4*)(l1b + d), b1 = *(const f32x4*)(l1b + d + 4);
;             f32x4 a0 = ((y0 - mean1) * rstd1 * g0 + b0) * DN_ALPHA, a1 = ((y1v - mean1) * rstd1 * g1 + b1) * DN_ALPHA;
; #pragma unroll
;             for (int k = 0; k < 4; ++k) { const u32x4 v = *(const u32x4*)(yb + ((size_t)tok * 4 + k) * D + d);
;                 a0[0] += bflo(v.x); a0[1] += bfhi(v.x); a0[2] += bflo(v.y); a0[3] += bfhi(v.y); a1[0] += bflo(v.z); a1[1] += bfhi(v.z); a1[2] += bflo(v.w); a1[3] += bfhi(v.w); }
;             z[2 * i] = a0; z[2 * i + 1] = a1; s += ((a0[0] + a0[1]) + (a0[2] + a0[3])) + ((a1[0] + a1[1]) + (a1[2] + a1[3])); }
.LBB0_977:
	v_lshl_add_u64 v[72:73], s[34:35], 0, v[70:71]
	v_add_co_u32_e64 v86, s[10:11], s24, v72
	s_waitcnt lgkmcnt(0)
	v_lshl_add_u64 v[0:1], s[34:35], 0, v[62:63]
	v_addc_co_u32_e64 v87, s[10:11], 0, v73, s[10:11]
	global_load_dwordx4 v[16:19], v[86:87], off
	v_add_co_u32_e64 v2, s[10:11], s25, v0
	s_nop 1
	v_addc_co_u32_e64 v3, s[10:11], 0, v1, s[10:11]
	v_add_co_u32_e64 v0, s[10:11], s26, v0
	global_load_dwordx4 v[78:81], v[2:3], off
	s_nop 0
	v_addc_co_u32_e64 v1, s[10:11], 0, v1, s[10:11]
	s_add_i32 s10, s5, s13
	s_ashr_i32 s11, s10, 31
	global_load_dwordx4 v[88:91], v[0:1], off offset:-4096
	global_load_dwordx4 v[102:105], v[0:1], off
	s_lshl_b64 s[10:11], s[10:11], 2
	s_add_u32 s10, s3, s10
	s_addc_u32 s11, s71, s11
	global_load_dwordx2 v[82:83], v58, s[10:11]
	global_load_dwordx4 v[106:109], v[2:3], off offset:-4096
	global_load_dwordx4 v[74:77], v[26:27], off
	global_load_dwordx4 v[110:113], v[24:25], off
	global_load_dwordx4 v[114:117], v[24:25], off offset:16
	global_load_dwordx4 v[118:121], v[26:27], off offset:16
	global_load_dwordx4 v[12:15], v[24:25], off offset:2064
	global_load_dwordx4 v[122:125], v[24:25], off offset:2048
	v_lshl_add_u64 v[0:1], s[34:35], 0, v[64:65]
	v_add_co_u32_e64 v4, s[10:11], s25, v0
	s_waitcnt vmcnt(11)
	v_lshlrev_b32_e32 v59, 16, v16
	v_addc_co_u32_e64 v5, s[10:11], 0, v1, s[10:11]
	v_add_co_u32_e64 v84, s[10:11], s26, v0
	v_and_b32_e32 v101, 0xffff0000, v16
	s_nop 0
	v_addc_co_u32_e64 v85, s[10:11], 0, v1, s[10:11]
	global_load_dwordx4 v[130:133], v[86:87], off offset:1024
	global_load_dwordx4 v[8:11], v[4:5], off offset:-4096
	global_load_dwordx4 v[0:3], v[4:5], off
	s_nop 0
	global_load_dwordx4 v[4:7], v[84:85], off offset:-4096
	v_lshlrev_b32_e32 v134, 16, v17
	v_and_b32_e32 v135, 0xffff0000, v17
	s_waitcnt vmcnt(11)
	v_sub_f32_e32 v135, v135, v82
	v_sub_f32_e32 v134, v134, v82
	v_sub_f32_e32 v137, v101, v82
	v_sub_f32_e32 v136, v59, v82
	v_pk_mul_f32 v[136:137], v[82:83], v[136:137] op_sel:[1,0]
	v_pk_mul_f32 v[134:135], v[82:83], v[134:135] op_sel:[1,0]
	s_waitcnt vmcnt(10)
	v_lshlrev_b32_e32 v142, 16, v106
	v_and_b32_e32 v143, 0xffff0000, v106
	v_lshlrev_b32_e32 v106, 16, v107
	v_and_b32_e32 v107, 0xffff0000, v107
	s_waitcnt vmcnt(8)
	v_pk_fma_f32 v[76:77], v[112:113], v[134:135], v[76:77]
	v_pk_fma_f32 v[74:75], v[110:111], v[136:137], v[74:75]
	v_lshlrev_b32_e32 v16, 16, v78
	v_and_b32_e32 v17, 0xffff0000, v78
	v_lshlrev_b32_e32 v78, 16, v79
	v_and_b32_e32 v79, 0xffff0000, v79
	v_pk_fma_f32 v[74:75], v[74:75], s[14:15], v[142:143] op_sel_hi:[1,0,1]
	v_pk_fma_f32 v[76:77], v[76:77], s[14:15], v[106:107] op_sel_hi:[1,0,1]
	v_lshlrev_b32_e32 v140, 16, v18
	v_and_b32_e32 v141, 0xffff0000, v18
	v_lshlrev_b32_e32 v138, 16, v19
	v_and_b32_e32 v139, 0xffff0000, v19
	v_lshlrev_b32_e32 v18, 16, v88
	v_and_b32_e32 v19, 0xffff0000, v88
	v_lshlrev_b32_e32 v88, 16, v89
	v_and_b32_e32 v89, 0xffff0000, v89
	v_pk_add_f32 v[16:17], v[74:75], v[16:17]
	v_pk_add_f32 v[74:75], v[76:77], v[78:79]
	v_lshlrev_b32_e32 v92, 16, v102
	v_and_b32_e32 v93, 0xffff0000, v102
	v_lshlrev_b32_e32 v102, 16, v103
	v_pk_add_f32 v[16:17], v[16:17], v[18:19]
	v_pk_add_f32 v[18:19], v[74:75], v[88:89]
	v_and_b32_e32 v103, 0xffff0000, v103
	v_pk_add_f32 v[74:75], v[16:17], v[92:93]
	v_pk_add_f32 v[76:77], v[18:19], v[102:103]
	global_load_dwordx4 v[16:19], v[84:85], off
	v_sub_f32_e32 v141, v141, v82
	v_sub_f32_e32 v140, v140, v82
	v_pk_mul_f32 v[140:141], v[82:83], v[140:141] op_sel:[1,0]
	v_lshlrev_b32_e32 v78, 16, v108
	s_waitcnt vmcnt(7)
	v_pk_fma_f32 v[112:113], v[114:115], v[140:141], v[118:119]
	v_and_b32_e32 v79, 0xffff0000, v108
	v_pk_fma_f32 v[78:79], v[112:113], s[14:15], v[78:79] op_sel_hi:[1,0,1]
	v_lshlrev_b32_e32 v84, 16, v80
	v_and_b32_e32 v85, 0xffff0000, v80
	v_sub_f32_e32 v139, v139, v82
	v_sub_f32_e32 v138, v138, v82
	v_pk_add_f32 v[78:79], v[78:79], v[84:85]
	v_lshlrev_b32_e32 v84, 16, v90
	v_and_b32_e32 v85, 0xffff0000, v90
	v_pk_mul_f32 v[138:139], v[82:83], v[138:139] op_sel:[1,0]
	v_pk_add_f32 v[78:79], v[78:79], v[84:85]
	v_lshlrev_b32_e32 v84, 16, v104
	v_and_b32_e32 v85, 0xffff0000, v104
	v_pk_fma_f32 v[110:111], v[116:117], v[138:139], v[120:121]
	v_pk_add_f32 v[78:79], v[78:79], v[84:85]
	v_lshlrev_b32_e32 v84, 16, v109
	v_and_b32_e32 v85, 0xffff0000, v109
	v_pk_fma_f32 v[84:85], v[110:111], s[14:15], v[84:85] op_sel_hi:[1,0,1]
	v_lshlrev_b32_e32 v80, 16, v81
	v_and_b32_e32 v81, 0xffff0000, v81
	v_pk_add_f32 v[80:81], v[84:85], v[80:81]
	v_lshlrev_b32_e32 v84, 16, v91
	v_and_b32_e32 v85, 0xffff0000, v91
	v_pk_add_f32 v[80:81], v[80:81], v[84:85]
	v_lshlrev_b32_e32 v84, 16, v105
	v_and_b32_e32 v85, 0xffff0000, v105
	v_pk_add_f32 v[80:81], v[80:81], v[84:85]
	v_mov_b32_e32 v84, v78
	v_mov_b32_e32 v85, v74
	v_mov_b32_e32 v88, v79
	v_mov_b32_e32 v89, v75
	v_pk_add_f32 v[84:85], v[84:85], v[88:89]
	v_mov_b32_e32 v88, v80
	v_mov_b32_e32 v89, v76
	v_mov_b32_e32 v90, v81
	v_mov_b32_e32 v91, v77
	v_pk_add_f32 v[88:89], v[88:89], v[90:91]
	s_waitcnt vmcnt(4)
	v_lshlrev_b32_e32 v59, 16, v130
	v_pk_add_f32 v[84:85], v[84:85], v[88:89]
	v_sub_f32_e32 v90, v59, v82
	v_pk_add_f32 v[88:89], v[84:85], v[84:85] op_sel:[0,1] op_sel_hi:[1,0]
	v_lshlrev_b32_e32 v84, 16, v131
	v_and_b32_e32 v89, 0xffff0000, v130
	v_and_b32_e32 v85, 0xffff0000, v131
	v_sub_f32_e32 v85, v85, v82
	v_sub_f32_e32 v84, v84, v82
	v_sub_f32_e32 v91, v89, v82
	v_lshlrev_b32_e32 v101, 16, v132
	v_and_b32_e32 v102, 0xffff0000, v132
	v_lshlrev_b32_e32 v103, 16, v133
	v_pk_mul_f32 v[90:91], v[82:83], v[90:91] op_sel:[1,0]
	v_pk_mul_f32 v[84:85], v[82:83], v[84:85] op_sel:[1,0]
	v_and_b32_e32 v104, 0xffff0000, v133
	v_pk_fma_f32 v[92:93], v[124:125], v[84:85], v[150:151]
	v_pk_fma_f32 v[84:85], v[122:123], v[90:91], v[148:149]
	v_sub_f32_e32 v90, v103, v82
	v_sub_f32_e32 v103, v102, v82
	v_sub_f32_e32 v102, v101, v82
	v_sub_f32_e32 v91, v104, v82
	v_pk_mul_f32 v[106:107], v[82:83], v[102:103] op_sel:[1,0]
	global_load_dwordx4 v[102:105], v[86:87], off offset:2048
	v_pk_fma_f32 v[122:123], v[12:13], v[106:107], v[144:145]
	v_pk_mul_f32 v[90:91], v[82:83], v[90:91] op_sel:[1,0]
	s_waitcnt vmcnt(4)
; DI float bflo(unsigned w) { return __uint_as_float(w << 16); }
; DI float bfhi(unsigned w) { return __uint_as_float(w & 0xffff0000u); }
; DI void p7_ln2(const Ctx& c) {
;     ...
;         for (int i = 0; i < 4; ++i) { const int d = (i * 64 + lane) * 8; const u32x4 yr = *(const u32x4*)(y1 + (size_t)tok * D + d);
;             const f32x4 y0 = {bflo(yr.x), bfhi(yr.x), bflo(yr.y), bfhi(yr.y)}, y1v = {bflo(yr.z), bfhi(yr.z), bflo(yr.w), bfhi(yr.w)};
;             const f32x4 g0 = *(const f32x4*)(l1w + d), g1 = *(const f32x4*)(l1w + d + 4), b0 = *(const f32x4*)(l1b + d), b1 = *(const f32x4*)(l1b + d + 4);
;             f32x4 a0 = ((y0 - mean1) * rstd1 * g0 + b0) * DN_ALPHA, a1 = ((y1v - mean1) * rstd1 * g1 + b1) * DN_ALPHA;
; #pragma unroll
;             for (int k = 0; k < 4; ++k) { const u32x4 v = *(const u32x4*)(yb + ((size_t)tok * 4 + k) * D + d);
;                 a0[0] += bflo(v.x); a0[1] += bfhi(v.x); a0[2] += bflo(v.y); a0[3] += bfhi(v.y); a1[0] += bflo(v.z); a1[1] += bfhi(v.z); a1[2] += bflo(v.w); a1[3] += bfhi(v.w); }
;             z[2 * i] = a0; z[2 * i + 1] = a1; s += ((a0[0] + a0[1]) + (a0[2] + a0[3])) + ((a1[0] + a1[1]) + (a1[2] + a1[3])); }
	v_lshlrev_b32_e32 v12, 16, v8
	v_and_b32_e32 v13, 0xffff0000, v8
	v_lshlrev_b32_e32 v8, 16, v9
	v_and_b32_e32 v9, 0xffff0000, v9
	v_pk_fma_f32 v[90:91], v[14:15], v[90:91], v[146:147]
	v_pk_fma_f32 v[12:13], v[84:85], s[14:15], v[12:13] op_sel_hi:[1,0,1]
	s_waitcnt vmcnt(3)
	v_lshlrev_b32_e32 v14, 16, v0
	v_and_b32_e32 v15, 0xffff0000, v0
	v_pk_fma_f32 v[8:9], v[92:93], s[14:15], v[8:9] op_sel_hi:[1,0,1]
	v_lshlrev_b32_e32 v0, 16, v1
	v_and_b32_e32 v1, 0xffff0000, v1
	v_pk_add_f32 v[12:13], v[12:13], v[14:15]
	s_waitcnt vmcnt(2)
	v_lshlrev_b32_e32 v14, 16, v4
	v_and_b32_e32 v15, 0xffff0000, v4
	v_pk_add_f32 v[0:1], v[8:9], v[0:1]
	v_lshlrev_b32_e32 v4, 16, v5
	v_and_b32_e32 v5, 0xffff0000, v5
	v_lshl_add_u64 v[124:125], s[34:35], 0, v[66:67]
	v_pk_add_f32 v[0:1], v[0:1], v[4:5]
	s_waitcnt vmcnt(1)
	v_lshlrev_b32_e32 v4, 16, v17
	v_and_b32_e32 v5, 0xffff0000, v17
	v_add_co_u32_e64 v22, s[10:11], s25, v124
	v_pk_add_f32 v[0:1], v[0:1], v[4:5]
	v_lshlrev_b32_e32 v4, 16, v10
	v_and_b32_e32 v5, 0xffff0000, v10
	v_addc_co_u32_e64 v23, s[10:11], 0, v125, s[10:11]
	v_pk_fma_f32 v[4:5], v[122:123], s[14:15], v[4:5] op_sel_hi:[1,0,1]
	v_lshlrev_b32_e32 v8, 16, v2
	v_and_b32_e32 v9, 0xffff0000, v2
	v_pk_add_f32 v[4:5], v[4:5], v[8:9]
	v_add_co_u32_e64 v8, s[10:11], s26, v124
	v_lshlrev_b32_e32 v84, 16, v16
	v_and_b32_e32 v85, 0xffff0000, v16
	v_addc_co_u32_e64 v9, s[10:11], 0, v125, s[10:11]
	v_lshlrev_b32_e32 v16, 16, v6
	v_and_b32_e32 v17, 0xffff0000, v6
	global_load_dwordx4 v[122:125], v[8:9], off offset:-4096
	global_load_dwordx4 v[126:129], v[8:9], off
	v_pk_add_f32 v[4:5], v[4:5], v[16:17]
	v_lshlrev_b32_e32 v8, 16, v18
	v_and_b32_e32 v9, 0xffff0000, v18
	v_pk_add_f32 v[4:5], v[4:5], v[8:9]
	v_lshlrev_b32_e32 v8, 16, v11
	v_and_b32_e32 v9, 0xffff0000, v11
	v_pk_fma_f32 v[8:9], v[90:91], s[14:15], v[8:9] op_sel_hi:[1,0,1]
	v_lshlrev_b32_e32 v2, 16, v3
	v_and_b32_e32 v3, 0xffff0000, v3
	v_pk_add_f32 v[20:21], v[12:13], v[14:15]
	global_load_dwordx4 v[12:15], v[22:23], off offset:-4096
	v_pk_add_f32 v[2:3], v[8:9], v[2:3]
	v_lshlrev_b32_e32 v6, 16, v7
	v_and_b32_e32 v7, 0xffff0000, v7
	v_pk_add_f32 v[84:85], v[20:21], v[84:85]
	v_pk_add_f32 v[2:3], v[2:3], v[6:7]
	v_lshlrev_b32_e32 v6, 16, v19
	v_and_b32_e32 v7, 0xffff0000, v19
	global_load_dwordx4 v[16:19], v[86:87], off offset:3072
	v_pk_add_f32 v[2:3], v[2:3], v[6:7]
	global_load_dwordx4 v[20:23], v[22:23], off
	v_mov_b32_e32 v6, v84
	v_mov_b32_e32 v7, v0
	v_mov_b32_e32 v8, v85
	v_mov_b32_e32 v9, v1
	v_pk_add_f32 v[6:7], v[6:7], v[8:9]
	v_mov_b32_e32 v8, v5
	v_pk_add_f32 v[90:91], v[6:7], v[6:7] op_sel:[0,1] op_sel_hi:[1,0]
	v_mov_b32_e32 v6, v4
	v_mov_b32_e32 v7, v2
	v_mov_b32_e32 v9, v3
	v_pk_add_f32 v[6:7], v[6:7], v[8:9]
	v_lshl_add_u64 v[134:135], s[34:35], 0, v[68:69]
	v_pk_add_f32 v[92:93], v[6:7], v[6:7] op_sel:[0,1] op_sel_hi:[1,0]
	s_waitcnt vmcnt(5)
	v_lshlrev_b32_e32 v8, 16, v102
	v_and_b32_e32 v9, 0xffff0000, v102
	v_lshlrev_b32_e32 v6, 16, v103
	v_and_b32_e32 v7, 0xffff0000, v103
	v_sub_f32_e32 v7, v7, v82
	v_sub_f32_e32 v6, v6, v82
	v_sub_f32_e32 v9, v9, v82
	v_sub_f32_e32 v8, v8, v82
	v_lshlrev_b32_e32 v59, 16, v104
	v_and_b32_e32 v86, 0xffff0000, v104
	v_lshlrev_b32_e32 v87, 16, v105
	v_and_b32_e32 v89, 0xffff0000, v105
	v_pk_mul_f32 v[8:9], v[82:83], v[8:9] op_sel:[1,0]
	v_pk_mul_f32 v[6:7], v[82:83], v[6:7] op_sel:[1,0]
	v_add_co_u32_e64 v130, s[10:11], s25, v134
	s_waitcnt vmcnt(5)
	v_pk_fma_f32 v[10:11], v[158:159], v[6:7], v[166:167]
	v_pk_fma_f32 v[6:7], v[156:157], v[8:9], v[164:165]
	v_sub_f32_e32 v9, v89, v82
	v_sub_f32_e32 v8, v87, v82
	v_sub_f32_e32 v87, v86, v82
	v_sub_f32_e32 v86, v59, v82
	v_pk_mul_f32 v[86:87], v[82:83], v[86:87] op_sel:[1,0]
	v_pk_mul_f32 v[8:9], v[82:83], v[8:9] op_sel:[1,0]
	v_pk_fma_f32 v[86:87], v[152:153], v[86:87], v[160:161]
	v_pk_fma_f32 v[142:143], v[154:155], v[8:9], v[162:163]
	v_addc_co_u32_e64 v131, s[10:11], 0, v135, s[10:11]
	v_add_co_u32_e64 v138, s[10:11], s26, v134
	global_load_dwordx4 v[118:121], v[130:131], off offset:-4096
	s_nop 0
	global_load_dwordx4 v[130:133], v[130:131], off
	v_addc_co_u32_e64 v139, s[10:11], 0, v135, s[10:11]
	global_load_dwordx4 v[134:137], v[138:139], off offset:-4096
	s_waitcnt vmcnt(5)
	v_lshlrev_b32_e32 v8, 16, v12
	global_load_dwordx4 v[138:141], v[138:139], off
	v_and_b32_e32 v9, 0xffff0000, v12
	v_pk_fma_f32 v[6:7], v[6:7], s[14:15], v[8:9] op_sel_hi:[1,0,1]
	s_waitcnt vmcnt(5)
	v_lshlrev_b32_e32 v59, 16, v19
	s_waitcnt vmcnt(4)
	v_lshlrev_b32_e32 v8, 16, v20
	v_and_b32_e32 v9, 0xffff0000, v20
	v_pk_add_f32 v[6:7], v[6:7], v[8:9]
	v_lshlrev_b32_e32 v8, 16, v122
	v_and_b32_e32 v9, 0xffff0000, v122
	v_pk_add_f32 v[6:7], v[6:7], v[8:9]
	v_lshlrev_b32_e32 v8, 16, v126
	v_and_b32_e32 v9, 0xffff0000, v126
	v_pk_add_f32 v[6:7], v[6:7], v[8:9]
	v_lshlrev_b32_e32 v8, 16, v13
	v_and_b32_e32 v9, 0xffff0000, v13
	v_pk_fma_f32 v[8:9], v[10:11], s[14:15], v[8:9] op_sel_hi:[1,0,1]
	v_lshlrev_b32_e32 v10, 16, v21
	v_and_b32_e32 v11, 0xffff0000, v21
	v_pk_add_f32 v[8:9], v[8:9], v[10:11]
	v_lshlrev_b32_e32 v10, 16, v123
	v_and_b32_e32 v11, 0xffff0000, v123
	v_pk_add_f32 v[8:9], v[8:9], v[10:11]
	v_lshlrev_b32_e32 v10, 16, v127
	v_and_b32_e32 v11, 0xffff0000, v127
	v_pk_add_f32 v[8:9], v[8:9], v[10:11]
	v_lshlrev_b32_e32 v10, 16, v14
	v_and_b32_e32 v11, 0xffff0000, v14
	v_pk_fma_f32 v[10:11], v[86:87], s[14:15], v[10:11] op_sel_hi:[1,0,1]
	v_lshlrev_b32_e32 v12, 16, v22
	v_and_b32_e32 v13, 0xffff0000, v22
	v_pk_add_f32 v[10:11], v[10:11], v[12:13]
	v_lshlrev_b32_e32 v12, 16, v124
	v_and_b32_e32 v13, 0xffff0000, v124
	v_pk_add_f32 v[10:11], v[10:11], v[12:13]
	v_lshlrev_b32_e32 v12, 16, v128
	v_and_b32_e32 v13, 0xffff0000, v128
	v_pk_add_f32 v[10:11], v[10:11], v[12:13]
	v_lshlrev_b32_e32 v12, 16, v15
	v_and_b32_e32 v13, 0xffff0000, v15
	v_pk_fma_f32 v[12:13], v[142:143], s[14:15], v[12:13] op_sel_hi:[1,0,1]
	v_lshlrev_b32_e32 v14, 16, v23
	v_and_b32_e32 v15, 0xffff0000, v23
	v_pk_add_f32 v[12:13], v[12:13], v[14:15]
	v_lshlrev_b32_e32 v14, 16, v125
	v_and_b32_e32 v15, 0xffff0000, v125
	v_pk_add_f32 v[12:13], v[12:13], v[14:15]
	v_lshlrev_b32_e32 v14, 16, v129
	v_and_b32_e32 v15, 0xffff0000, v129
	v_pk_add_f32 v[12:13], v[12:13], v[14:15]
	v_lshlrev_b32_e32 v20, 16, v16
	v_and_b32_e32 v16, 0xffff0000, v16
	v_lshlrev_b32_e32 v14, 16, v17
	v_and_b32_e32 v15, 0xffff0000, v17
	v_pk_add_f32 v[86:87], v[8:9], v[8:9] op_sel:[0,1] op_sel_hi:[1,0]
	v_sub_f32_e32 v15, v15, v82
	v_sub_f32_e32 v14, v14, v82
	v_sub_f32_e32 v17, v16, v82
	v_sub_f32_e32 v16, v20, v82
	v_pk_add_f32 v[22:23], v[6:7], v[6:7] op_sel:[0,1] op_sel_hi:[1,0]
	v_and_b32_e32 v87, 0xffff0000, v19
	v_pk_mul_f32 v[16:17], v[82:83], v[16:17] op_sel:[1,0]
	v_pk_mul_f32 v[14:15], v[82:83], v[14:15] op_sel:[1,0]
	v_lshlrev_b32_e32 v23, 16, v18
	v_and_b32_e32 v21, 0xffff0000, v18
	s_waitcnt vmcnt(4)
; DI void p7_ln2(const Ctx& c) {
;     ...
;             z[2 * i] = a0; z[2 * i + 1] = a1; s += ((a0[0] + a0[1]) + (a0[2] + a0[3])) + ((a1[0] + a1[1]) + (a1[2] + a1[3])); }
; #pragma unroll
;         for (int o = 32; o >= 1; o >>= 1) s += __shfl_xor(s, o);
;         const float mean = s * (1.0f / D); float qv = 0.f;
; #pragma unroll
;         for (int i = 0; i < 8; ++i) { const f32x4 dl = z[i] - mean; qv += (dl[0] * dl[0] + dl[1] * dl[1]) + (dl[2] * dl[2] + dl[3] * dl[3]); }
	v_pk_fma_f32 v[18:19], v[174:175], v[14:15], v[182:183]
	v_pk_fma_f32 v[14:15], v[172:173], v[16:17], v[180:181]
	v_sub_f32_e32 v17, v87, v82
	v_sub_f32_e32 v16, v59, v82
	v_sub_f32_e32 v21, v21, v82
	v_sub_f32_e32 v20, v23, v82
	v_pk_mul_f32 v[16:17], v[82:83], v[16:17] op_sel:[1,0]
	v_pk_mul_f32 v[20:21], v[82:83], v[20:21] op_sel:[1,0]
	v_pk_fma_f32 v[82:83], v[170:171], v[16:17], v[178:179]
	s_waitcnt vmcnt(3)
	v_lshlrev_b32_e32 v16, 16, v118
	v_and_b32_e32 v17, 0xffff0000, v118
	v_pk_fma_f32 v[14:15], v[14:15], s[14:15], v[16:17] op_sel_hi:[1,0,1]
	s_waitcnt vmcnt(2)
	v_lshlrev_b32_e32 v16, 16, v130
	v_and_b32_e32 v17, 0xffff0000, v130
	v_pk_add_f32 v[14:15], v[14:15], v[16:17]
	s_waitcnt vmcnt(1)
	v_lshlrev_b32_e32 v16, 16, v134
	v_and_b32_e32 v17, 0xffff0000, v134
	v_pk_add_f32 v[14:15], v[14:15], v[16:17]
	s_waitcnt vmcnt(0)
	v_lshlrev_b32_e32 v16, 16, v138
	v_and_b32_e32 v17, 0xffff0000, v138
	v_pk_add_f32 v[14:15], v[14:15], v[16:17]
	v_lshlrev_b32_e32 v16, 16, v119
	v_and_b32_e32 v17, 0xffff0000, v119
	v_pk_fma_f32 v[16:17], v[18:19], s[14:15], v[16:17] op_sel_hi:[1,0,1]
	v_lshlrev_b32_e32 v18, 16, v131
	v_and_b32_e32 v19, 0xffff0000, v131
	v_pk_add_f32 v[16:17], v[16:17], v[18:19]
	v_lshlrev_b32_e32 v18, 16, v135
	v_and_b32_e32 v19, 0xffff0000, v135
	v_pk_add_f32 v[16:17], v[16:17], v[18:19]
	v_lshlrev_b32_e32 v18, 16, v139
	v_and_b32_e32 v19, 0xffff0000, v139
	v_pk_fma_f32 v[20:21], v[168:169], v[20:21], v[176:177]
	v_pk_add_f32 v[16:17], v[16:17], v[18:19]
	v_lshlrev_b32_e32 v18, 16, v120
	v_and_b32_e32 v19, 0xffff0000, v120
	v_pk_fma_f32 v[18:19], v[20:21], s[14:15], v[18:19] op_sel_hi:[1,0,1]
	v_lshlrev_b32_e32 v20, 16, v132
	v_and_b32_e32 v21, 0xffff0000, v132
	v_pk_add_f32 v[18:19], v[18:19], v[20:21]
	v_lshlrev_b32_e32 v20, 16, v136
	v_and_b32_e32 v21, 0xffff0000, v136
	v_pk_add_f32 v[18:19], v[18:19], v[20:21]
	v_lshlrev_b32_e32 v20, 16, v140
	v_and_b32_e32 v21, 0xffff0000, v140
	v_pk_add_f32 v[18:19], v[18:19], v[20:21]
	v_lshlrev_b32_e32 v20, 16, v121
	v_and_b32_e32 v21, 0xffff0000, v121
	v_pk_fma_f32 v[20:21], v[82:83], s[14:15], v[20:21] op_sel_hi:[1,0,1]
	v_lshlrev_b32_e32 v82, 16, v133
	v_and_b32_e32 v83, 0xffff0000, v133
	v_pk_add_f32 v[20:21], v[20:21], v[82:83]
	v_lshlrev_b32_e32 v82, 16, v137
	v_and_b32_e32 v83, 0xffff0000, v137
	v_pk_add_f32 v[122:123], v[10:11], v[10:11] op_sel:[0,1] op_sel_hi:[1,0]
	v_pk_add_f32 v[124:125], v[12:13], v[12:13] op_sel:[0,1] op_sel_hi:[1,0]
	v_pk_add_f32 v[20:21], v[20:21], v[82:83]
	v_lshlrev_b32_e32 v82, 16, v141
	v_and_b32_e32 v83, 0xffff0000, v141
	v_pk_add_f32 v[20:21], v[20:21], v[82:83]
	v_mov_b32_e32 v123, v14
	v_mov_b32_e32 v125, v15
	v_mov_b32_e32 v23, v16
	v_mov_b32_e32 v87, v17
	v_pk_add_f32 v[82:83], v[122:123], v[124:125]
	v_pk_add_f32 v[22:23], v[22:23], v[86:87]
	v_mov_b32_e32 v89, v18
	v_mov_b32_e32 v59, v19
	v_mov_b32_e32 v93, v20
	v_mov_b32_e32 v91, v21
	v_pk_add_f32 v[22:23], v[82:83], v[22:23]
	v_pk_add_f32 v[82:83], v[88:89], v[58:59]
	v_pk_add_f32 v[86:87], v[92:93], v[90:91]
	s_nop 0
	v_pk_add_f32 v[82:83], v[82:83], v[86:87]
	s_nop 0
	v_pk_add_f32 v[22:23], v[82:83], v[22:23]
	s_nop 0
	v_add_f32_e32 v22, v22, v23
	v_mov_b32_e32 v23, v22
	s_nop 1
	v_permlane32_swap_b32 v22, v23
	v_add_f32_e32 v22, v22, v23
	v_mov_b32_e32 v23, v22
	s_nop 1
	v_permlane16_swap_b32 v22, v23
	v_add_f32_e32 v22, v22, v23
	s_nop 1
	v_add_f32_dpp v22, v22, v22 row_ror:8 row_mask:0xf bank_mask:0xf
	s_nop 1
	v_add_f32_dpp v22, v22, v22 row_ror:4 row_mask:0xf bank_mask:0xf
	s_nop 1
	v_add_f32_dpp v22, v22, v22 quad_perm:[2,3,0,1] row_mask:0xf bank_mask:0xf
	s_nop 1
	v_add_f32_dpp v59, v22, v22 quad_perm:[1,0,3,2] row_mask:0xf bank_mask:0xf
	v_fmamk_f32 v75, v59, 0xba000000, v75
	v_fmamk_f32 v79, v59, 0xba000000, v79
	v_fmamk_f32 v77, v59, 0xba000000, v77
	v_fmac_f32_e32 v74, 0xba000000, v59
	v_fmamk_f32 v81, v59, 0xba000000, v81
	v_fmac_f32_e32 v78, 0xba000000, v59
	v_mov_b32_e32 v82, v75
	v_mov_b32_e32 v83, v79
	v_fmac_f32_e32 v76, 0xba000000, v59
	v_fmac_f32_e32 v80, 0xba000000, v59
	v_mov_b32_e32 v22, v74
	v_mov_b32_e32 v23, v78
	v_pk_mul_f32 v[82:83], v[82:83], v[82:83]
	v_mov_b32_e32 v86, v77
	v_mov_b32_e32 v87, v81
	v_pk_fma_f32 v[22:23], v[22:23], v[22:23], v[82:83]
	v_mov_b32_e32 v82, v76
	v_mov_b32_e32 v83, v80
	v_pk_mul_f32 v[86:87], v[86:87], v[86:87]
	v_fmamk_f32 v85, v59, 0xba000000, v85
	v_pk_fma_f32 v[82:83], v[82:83], v[82:83], v[86:87]
	v_fmac_f32_e32 v84, 0xba000000, v59
	v_pk_add_f32 v[22:23], v[22:23], v[82:83]
	v_fmamk_f32 v1, v59, 0xba000000, v1
	v_fmac_f32_e32 v0, 0xba000000, v59
	v_pk_add_f32 v[22:23], v[22:23], v[22:23] op_sel_hi:[0,1]
	v_pk_mul_f32 v[82:83], v[0:1], v[0:1]
	v_pk_mul_f32 v[86:87], v[84:85], v[84:85]
	v_fmac_f32_e32 v4, 0xba000000, v59
	v_pk_mov_b32 v[88:89], v[86:87], v[82:83] op_sel:[1,0]
	v_mov_b32_e32 v87, v83
	v_fmamk_f32 v5, v59, 0xba000000, v5
	v_fmac_f32_e32 v2, 0xba000000, v59
	v_mul_f32_e32 v22, v4, v4
	v_pk_add_f32 v[82:83], v[88:89], v[86:87]
	v_fmamk_f32 v3, v59, 0xba000000, v3
	v_pk_fma_f32 v[86:87], v[4:5], v[4:5], v[22:23] op_sel_hi:[1,1,0]
	v_mul_f32_e32 v22, v2, v2
	v_pk_add_f32 v[82:83], v[82:83], v[82:83] op_sel_hi:[0,1]
	v_pk_fma_f32 v[88:89], v[2:3], v[2:3], v[22:23] op_sel_hi:[1,1,0]
	v_fmamk_f32 v9, v59, 0xba000000, v9
	v_fmac_f32_e32 v8, 0xba000000, v59
	v_fmamk_f32 v7, v59, 0xba000000, v7
	v_fmac_f32_e32 v6, 0xba000000, v59
	v_mul_f32_e32 v86, v6, v6
	v_mul_f32_e32 v88, v7, v7
	v_mul_f32_e32 v82, v8, v8
	v_mul_f32_e32 v22, v9, v9
	v_pk_add_f32 v[86:87], v[86:87], v[88:89]
	v_pk_add_f32 v[22:23], v[82:83], v[22:23]
	v_fmamk_f32 v11, v59, 0xba000000, v11
	v_pk_add_f32 v[22:23], v[86:87], v[22:23]
; DI u32x2 pack4(f32x4 v) { bf16x4_t r = __builtin_convertvector(v, bf16x4_t); return __builtin_bit_cast(u32x2, r); }
; DI void p7_ln2(const Ctx& c) {
;     ...
;         for (int i = 0; i < 8; ++i) { const f32x4 dl = z[i] - mean; qv += (dl[0] * dl[0] + dl[1] * dl[1]) + (dl[2] * dl[2] + dl[3] * dl[3]); }
; #pragma unroll
;         for (int o = 32; o >= 1; o >>= 1) qv += __shfl_xor(qv, o);
;         const float rstd = rsqrtf(qv * (1.0f / D) + LN_EPS);
; #pragma unroll
;         for (int i = 0; i < 4; ++i) { const int d = (i * 64 + lane) * 8;
;             const f32x4 g0 = *(const f32x4*)(l2w + d), g1 = *(const f32x4*)(l2w + d + 4), b0 = *(const f32x4*)(l2b + d), b1 = *(const f32x4*)(l2b + d + 4);
;             const u32x2 lo = pack4((z[2 * i] - mean) * rstd * g0 + b0), hi = pack4((z[2 * i + 1] - mean) * rstd * g1 + b1);
;             *(u32x4*)(x2b + (size_t)tok * D + d) = (u32x4){lo.x, lo.y, hi.x, hi.y}; }
;         float q2 = (lane < 32) ? ssq[(size_t)tok * 32 + lane] : 0.f;
; #pragma unroll
;         for (int o = 32; o >= 1; o >>= 1) q2 += __shfl_xor(q2, o);
;         if (lane == 0) rse[tok] = rsqrtf(q2 * (1.0f / D) + LN_EPS); }
	v_fmac_f32_e32 v10, 0xba000000, v59
	v_fmamk_f32 v13, v59, 0xba000000, v13
	v_fmac_f32_e32 v12, 0xba000000, v59
	v_pk_add_f32 v[22:23], v[22:23], v[22:23] op_sel_hi:[0,1]
	v_pk_mul_f32 v[82:83], v[12:13], v[12:13]
	v_pk_mul_f32 v[110:111], v[10:11], v[10:11]
	v_fmac_f32_e32 v14, 0xba000000, v59
	v_pk_mov_b32 v[112:113], v[110:111], v[82:83] op_sel:[1,0]
	v_mov_b32_e32 v111, v83
	v_fmamk_f32 v15, v59, 0xba000000, v15
	v_fmac_f32_e32 v16, 0xba000000, v59
	v_mul_f32_e32 v22, v14, v14
	v_pk_add_f32 v[82:83], v[112:113], v[110:111]
	v_fmamk_f32 v17, v59, 0xba000000, v17
	v_pk_fma_f32 v[110:111], v[14:15], v[14:15], v[22:23] op_sel_hi:[1,1,0]
	v_mul_f32_e32 v22, v16, v16
	v_pk_add_f32 v[82:83], v[82:83], v[82:83] op_sel_hi:[0,1]
	v_pk_fma_f32 v[112:113], v[16:17], v[16:17], v[22:23] op_sel_hi:[1,1,0]
	v_fmamk_f32 v21, v59, 0xba000000, v21
	v_fmac_f32_e32 v20, 0xba000000, v59
	v_fmamk_f32 v19, v59, 0xba000000, v19
	v_fmac_f32_e32 v18, 0xba000000, v59
	v_mul_f32_e32 v110, v18, v18
	v_mul_f32_e32 v112, v19, v19
	v_mul_f32_e32 v82, v20, v20
	v_mul_f32_e32 v22, v21, v21
	v_pk_add_f32 v[110:111], v[110:111], v[112:113]
	v_pk_add_f32 v[22:23], v[82:83], v[22:23]
	s_nop 0
	v_pk_add_f32 v[22:23], v[110:111], v[22:23]
	s_nop 0
	v_add_f32_e32 v22, v22, v23
	v_mov_b32_e32 v23, v22
	s_nop 1
	v_permlane32_swap_b32 v22, v23
	v_add_f32_e32 v22, v22, v23
	v_mov_b32_e32 v23, v22
	s_nop 1
	v_permlane16_swap_b32 v22, v23
	v_add_f32_e32 v22, v22, v23
	s_nop 1
	v_add_f32_dpp v22, v22, v22 row_ror:8 row_mask:0xf bank_mask:0xf
	s_nop 1
	v_add_f32_dpp v22, v22, v22 row_ror:4 row_mask:0xf bank_mask:0xf
	s_nop 1
	v_add_f32_dpp v22, v22, v22 quad_perm:[2,3,0,1] row_mask:0xf bank_mask:0xf
	s_nop 1
	v_add_f32_dpp v22, v22, v22 quad_perm:[1,0,3,2] row_mask:0xf bank_mask:0xf
	v_fmamk_f32 v22, v22, 0x3a000000, v100
	v_mul_f32_e32 v23, 0x4b800000, v22
	v_cmp_gt_f32_e64 s[10:11], s27, v22
	s_nop 1
	v_cndmask_b32_e64 v22, v22, v23, s[10:11]
	v_rsq_f32_e32 v22, v22
	s_nop 0
	v_mul_f32_e32 v23, 0x45800000, v22
	v_cndmask_b32_e64 v22, v22, v23, s[10:11]
	v_pk_mul_f32 v[76:77], v[76:77], v[22:23] op_sel_hi:[1,0]
	v_pk_mul_f32 v[74:75], v[74:75], v[22:23] op_sel_hi:[1,0]
	v_pk_mul_f32 v[78:79], v[78:79], v[22:23] op_sel_hi:[1,0]
	s_waitcnt vmcnt(0)
	v_pk_fma_f32 v[82:83], v[188:189], v[74:75], v[196:197]
	v_pk_fma_f32 v[74:75], v[190:191], v[76:77], v[198:199]
	v_pk_mul_f32 v[76:77], v[80:81], v[22:23] op_sel_hi:[1,0]
	v_pk_fma_f32 v[78:79], v[184:185], v[78:79], v[192:193]
	v_pk_fma_f32 v[76:77], v[186:187], v[76:77], v[194:195]
	v_add_co_u32_e64 v90, s[10:11], s28, v72
	v_cvt_pk_bf16_f32 v75, v74, v75
	v_cvt_pk_bf16_f32 v74, v82, v83
	v_cvt_pk_bf16_f32 v77, v76, v77
	v_cvt_pk_bf16_f32 v76, v78, v79
	v_addc_co_u32_e64 v91, s[10:11], 0, v73, s[10:11]
	global_store_dwordx4 v[90:91], v[74:77], off
	s_nop 0
	v_pk_mul_f32 v[84:85], v[84:85], v[22:23] op_sel_hi:[1,0]
	v_pk_mul_f32 v[0:1], v[0:1], v[22:23] op_sel_hi:[1,0]
	v_pk_mul_f32 v[4:5], v[4:5], v[22:23] op_sel_hi:[1,0]
	v_pk_mul_f32 v[2:3], v[2:3], v[22:23] op_sel_hi:[1,0]
	s_waitcnt vmcnt(1)
	v_pk_fma_f32 v[74:75], v[206:207], v[0:1], v[202:203]
	v_pk_fma_f32 v[0:1], v[204:205], v[84:85], v[200:201]
	s_waitcnt vmcnt(1)
	v_pk_fma_f32 v[72:73], v[210:211], v[2:3], v[218:219]
	v_pk_fma_f32 v[2:3], v[208:209], v[4:5], v[216:217]
	v_cvt_pk_bf16_f32 v0, v0, v1
	v_cvt_pk_bf16_f32 v1, v74, v75
	v_cvt_pk_bf16_f32 v2, v2, v3
	v_cvt_pk_bf16_f32 v3, v72, v73
	global_store_dwordx4 v[90:91], v[0:3], off offset:1024
	s_nop 0
	v_pk_mul_f32 v[4:5], v[6:7], v[22:23] op_sel_hi:[1,0]
	v_pk_mul_f32 v[6:7], v[8:9], v[22:23] op_sel_hi:[1,0]
	s_waitcnt vmcnt(2)
	v_pk_fma_f32 v[0:1], v[224:225], v[4:5], v[220:221]
	v_pk_fma_f32 v[2:3], v[226:227], v[6:7], v[222:223]
	v_cvt_pk_bf16_f32 v0, v0, v1
	v_cvt_pk_bf16_f32 v1, v2, v3
	v_pk_mul_f32 v[2:3], v[10:11], v[22:23] op_sel_hi:[1,0]
	v_pk_mul_f32 v[4:5], v[12:13], v[22:23] op_sel_hi:[1,0]
	s_waitcnt vmcnt(2)
	v_pk_fma_f32 v[2:3], v[230:231], v[2:3], v[234:235]
	v_pk_fma_f32 v[4:5], v[232:233], v[4:5], v[236:237]
	v_cvt_pk_bf16_f32 v2, v2, v3
	v_cvt_pk_bf16_f32 v3, v4, v5
	global_store_dwordx4 v[90:91], v[0:3], off offset:2048
	s_nop 0
	v_pk_mul_f32 v[12:13], v[14:15], v[22:23] op_sel_hi:[1,0]
	v_pk_mul_f32 v[14:15], v[16:17], v[22:23] op_sel_hi:[1,0]
	s_waitcnt vmcnt(3)
	v_pk_fma_f32 v[0:1], v[244:245], v[12:13], v[238:239]
	v_pk_fma_f32 v[2:3], v[246:247], v[14:15], v[240:241]
	v_cvt_pk_bf16_f32 v0, v0, v1
	v_cvt_pk_bf16_f32 v1, v2, v3
	v_pk_mul_f32 v[2:3], v[18:19], v[22:23] op_sel_hi:[1,0]
	v_pk_mul_f32 v[4:5], v[20:21], v[22:23] op_sel_hi:[1,0]
	s_waitcnt vmcnt(3)
	v_pk_fma_f32 v[2:3], v[248:249], v[2:3], v[252:253]
	v_pk_fma_f32 v[4:5], v[250:251], v[4:5], v[254:255]
	v_cvt_pk_bf16_f32 v2, v2, v3
	v_cvt_pk_bf16_f32 v3, v4, v5
	global_store_dwordx4 v[90:91], v[0:3], off offset:3072
	s_nop 1
	v_mov_b32_e32 v0, 0
	s_and_saveexec_b64 s[10:11], vcc
	s_cbranch_execz .LBB0_979
	v_lshl_add_u64 v[0:1], s[34:35], 0, v[60:61]
	global_load_dword v0, v[0:1], off
.LBB0_979:
	s_or_b64 exec, exec, s[10:11]
	s_waitcnt vmcnt(0)
	v_mov_b32_e32 v1, v0
	s_nop 1
	v_permlane32_swap_b32 v0, v1
	v_add_f32_e32 v0, v0, v1
	v_mov_b32_e32 v1, v0
	s_nop 1
	v_permlane16_swap_b32 v0, v1
	v_add_f32_e32 v0, v0, v1
	s_nop 1
	v_add_f32_dpp v0, v0, v0 row_ror:8 row_mask:0xf bank_mask:0xf
	s_nop 1
	v_add_f32_dpp v0, v0, v0 row_ror:4 row_mask:0xf bank_mask:0xf
	s_nop 1
	v_add_f32_dpp v0, v0, v0 quad_perm:[2,3,0,1] row_mask:0xf bank_mask:0xf
	ds_bpermute_b32 v1, v99, v0
	s_and_saveexec_b64 s[22:23], s[6:7]
	s_cbranch_execz .LBB0_976
	s_waitcnt lgkmcnt(0)
	v_add_f32_e32 v0, v0, v1
	v_fmamk_f32 v0, v0, 0x3a000000, v100
	v_mul_f32_e32 v1, 0x4b800000, v0
	v_cmp_gt_f32_e64 s[10:11], s27, v0
	s_add_u32 s36, s34, s30
	s_addc_u32 s37, s35, s31
	v_cndmask_b32_e64 v0, v0, v1, s[10:11]
	v_rsq_f32_e32 v0, v0
	s_nop 0
	v_mul_f32_e32 v1, 0x45800000, v0
	v_cndmask_b32_e64 v0, v0, v1, s[10:11]
	global_store_dword v58, v0, s[36:37]
	s_branch .LBB0_976
